# v50 + DPP/permlane instead of LDS round trips: all 62 ds_bpermute xor-shuffles per trip of the router phase replaced in place by DPP quad_perm / row_ror / half-mirror and double v_permlane16/32_swap
# baseline (speedup 1.0000x reference)
.LBB0_485:
	v_lshlrev_b32_e32 v18, 16, v16
	v_and_b32_e32 v19, 0xffff0000, v16
	v_lshlrev_b32_e32 v16, 16, v17
	v_and_b32_e32 v17, 0xffff0000, v17
	v_mul_f32_e32 v0, v19, v19
	v_mul_f32_e32 v1, v17, v17
	v_fmac_f32_e32 v0, v18, v18
	v_fmac_f32_e32 v1, v16, v16
	v_lshlrev_b32_e32 v20, 16, v14
	v_and_b32_e32 v21, 0xffff0000, v14
	v_lshlrev_b32_e32 v14, 16, v15
	v_and_b32_e32 v15, 0xffff0000, v15
	v_add_f32_e32 v0, v0, v1
	v_mul_f32_e32 v1, v21, v21
	v_mul_f32_e32 v22, v15, v15
	v_fmac_f32_e32 v1, v20, v20
	v_fmac_f32_e32 v22, v14, v14
	v_add_f32_e32 v1, v1, v22
	v_lshlrev_b32_e32 v22, 16, v12
	v_and_b32_e32 v23, 0xffff0000, v12
	v_lshlrev_b32_e32 v12, 16, v13
	v_and_b32_e32 v13, 0xffff0000, v13
	v_add_f32_e32 v0, v0, v1
	v_mul_f32_e32 v1, v23, v23
	v_mul_f32_e32 v24, v13, v13
	v_fmac_f32_e32 v1, v22, v22
	v_fmac_f32_e32 v24, v12, v12
	v_add_f32_e32 v1, v1, v24
	v_lshlrev_b32_e32 v24, 16, v10
	v_and_b32_e32 v25, 0xffff0000, v10
	v_lshlrev_b32_e32 v10, 16, v11
	v_and_b32_e32 v11, 0xffff0000, v11
	v_add_f32_e32 v0, v0, v1
	v_mul_f32_e32 v1, v25, v25
	v_mul_f32_e32 v26, v11, v11
	v_fmac_f32_e32 v1, v24, v24
	v_fmac_f32_e32 v26, v10, v10
	v_add_f32_e32 v1, v1, v26
	v_add_f32_e32 v28, v0, v1
	s_nop 1
	v_mov_b32_dpp v30, v28 quad_perm:[1,0,3,2] row_mask:0xf bank_mask:0xf
	v_lshlrev_b32_e32 v0, 16, v8
	v_and_b32_e32 v1, 0xffff0000, v8
	v_lshlrev_b32_e32 v8, 16, v9
	v_and_b32_e32 v9, 0xffff0000, v9
	s_waitcnt lgkmcnt(0)
	v_add_f32_e32 v28, v28, v30
	s_nop 1
	v_mov_b32_dpp v30, v28 quad_perm:[2,3,0,1] row_mask:0xf bank_mask:0xf
	v_mul_f32_e32 v26, v1, v1
	v_mul_f32_e32 v27, v9, v9
	v_fmac_f32_e32 v26, v0, v0
	v_fmac_f32_e32 v27, v8, v8
	s_waitcnt lgkmcnt(0)
	v_add_f32_e32 v30, v28, v30
	s_nop 1
	v_mov_b32_dpp v160, v30 row_half_mirror row_mask:0xf bank_mask:0xf
	s_nop 1
	v_mov_b32_dpp v75, v160 quad_perm:[3,2,1,0] row_mask:0xf bank_mask:0xf
	v_add_f32_e32 v29, v26, v27
	v_lshlrev_b32_e32 v26, 16, v6
	v_and_b32_e32 v27, 0xffff0000, v6
	v_lshlrev_b32_e32 v6, 16, v7
	v_and_b32_e32 v7, 0xffff0000, v7
	v_mul_f32_e32 v31, v27, v27
	v_mul_f32_e32 v74, v7, v7
	v_fmac_f32_e32 v31, v26, v26
	v_fmac_f32_e32 v74, v6, v6
	v_add_f32_e32 v28, v31, v74
	v_add_f32_e32 v74, v29, v28
	v_lshlrev_b32_e32 v28, 16, v4
	v_and_b32_e32 v29, 0xffff0000, v4
	s_waitcnt lgkmcnt(0)
	v_add_f32_e32 v4, v30, v75
	s_nop 1
	v_mov_b32_dpp v75, v4 row_ror:8 row_mask:0xf bank_mask:0xf
	v_and_b32_e32 v31, 0xffff0000, v5
	v_lshlrev_b32_e32 v30, 16, v5
	v_mul_f32_e32 v5, v29, v29
	v_mul_f32_e32 v76, v31, v31
	s_waitcnt lgkmcnt(0)
	v_add_f32_e32 v4, v4, v75
	s_nop 1
	v_mov_b32_e32 v160, v4
	v_mov_b32_e32 v161, v4
	s_nop 1
	v_permlane16_swap_b32_e32 v160, v161
	s_nop 1
	v_permlane16_swap_b32_e32 v161, v160
	v_mov_b32_e32 v75, v161
	v_fmac_f32_e32 v5, v28, v28
	v_fmac_f32_e32 v76, v30, v30
	v_add_f32_e32 v5, v5, v76
	v_add_f32_e32 v5, v74, v5
	s_waitcnt lgkmcnt(0)
	v_add_f32_e32 v4, v4, v75
	s_nop 1
	v_mov_b32_e32 v160, v4
	v_mov_b32_e32 v161, v4
	s_nop 1
	v_permlane32_swap_b32_e32 v160, v161
	s_nop 1
	v_permlane32_swap_b32_e32 v161, v160
	v_mov_b32_e32 v74, v161
	v_lshlrev_b32_e32 v86, 16, v2
	v_and_b32_e32 v87, 0xffff0000, v2
	v_lshlrev_b32_e32 v88, 16, v3
	v_and_b32_e32 v89, 0xffff0000, v3
	s_waitcnt lgkmcnt(0)
	v_add_f32_e32 v2, v4, v74
	v_fmamk_f32 v2, v2, 0x3a800000, v119
	v_mul_f32_e32 v3, 0x4f800000, v2
	v_cmp_gt_f32_e32 vcc, s27, v2
	v_mul_f32_e32 v4, v87, v87
	v_mul_f32_e32 v74, v89, v89
	v_cndmask_b32_e32 v2, v2, v3, vcc
	v_sqrt_f32_e32 v3, v2
	v_fmac_f32_e32 v4, v86, v86
	v_fmac_f32_e32 v74, v88, v88
	v_add_f32_e32 v4, v4, v74
	v_add_u32_e32 v75, -1, v3
	v_fma_f32 v76, -v75, v3, v2
	v_cmp_ge_f32_e64 s[14:15], 0, v76
	v_add_u32_e32 v76, 1, v3
	s_nop 0
	v_cndmask_b32_e64 v75, v3, v75, s[14:15]
	v_fma_f32 v3, -v76, v3, v2
	v_cmp_lt_f32_e64 s[14:15], 0, v3
	s_nop 1
	v_cndmask_b32_e64 v3, v75, v76, s[14:15]
	v_mul_f32_e32 v75, 0x37800000, v3
	v_cndmask_b32_e32 v3, v3, v75, vcc
	v_cmp_class_f32_e32 vcc, v2, v120
	v_add_f32_e32 v76, v5, v4
	s_nop 1
	v_mov_b32_dpp v77, v76 quad_perm:[1,0,3,2] row_mask:0xf bank_mask:0xf
	v_cndmask_b32_e32 v2, v3, v2, vcc
	v_div_scale_f32 v3, s[14:15], v2, v2, 1.0
	v_rcp_f32_e32 v75, v3
	s_nop 0
	v_fma_f32 v4, -v3, v75, 1.0
	v_fmac_f32_e32 v75, v4, v75
	v_div_scale_f32 v4, vcc, 1.0, v2, 1.0
	v_mul_f32_e32 v5, v4, v75
	v_fma_f32 v74, -v3, v5, v4
	v_fmac_f32_e32 v5, v74, v75
	v_fma_f32 v3, -v3, v5, v4
	v_div_fmas_f32 v3, v3, v75, v5
	v_div_fixup_f32 v74, v3, v2, 1.0
	v_pk_mul_f32 v[2:3], v[16:17], v[74:75] op_sel_hi:[1,0]
	s_waitcnt lgkmcnt(0)
	v_add_f32_e32 v16, v76, v77
	s_nop 1
	v_mov_b32_dpp v17, v16 quad_perm:[2,3,0,1] row_mask:0xf bank_mask:0xf
	v_pk_mul_f32 v[4:5], v[18:19], v[74:75] op_sel_hi:[1,0]
	v_pk_mul_f32 v[96:97], v[34:35], v[2:3]
	v_pk_mul_f32 v[94:95], v[32:33], v[4:5]
	v_pk_add_f32 v[4:5], v[96:97], v[96:97]
	s_waitcnt lgkmcnt(0)
	v_add_f32_e32 v16, v16, v17
	s_nop 1
	v_mov_b32_dpp v160, v16 row_half_mirror row_mask:0xf bank_mask:0xf
	s_nop 1
	v_mov_b32_dpp v17, v160 quad_perm:[3,2,1,0] row_mask:0xf bank_mask:0xf
	v_pk_add_f32 v[2:3], v[94:95], v[94:95]
	ds_write_b128 v121, v[2:5]
	v_pk_mul_f32 v[2:3], v[14:15], v[74:75] op_sel_hi:[1,0]
	v_pk_mul_f32 v[4:5], v[20:21], v[74:75] op_sel_hi:[1,0]
	s_waitcnt lgkmcnt(1)
	v_add_f32_e32 v14, v16, v17
	s_nop 1
	v_mov_b32_dpp v15, v14 row_ror:8 row_mask:0xf bank_mask:0xf
	v_pk_mul_f32 v[98:99], v[36:37], v[4:5]
	v_pk_mul_f32 v[100:101], v[38:39], v[2:3]
	v_pk_add_f32 v[2:3], v[98:99], v[98:99]
	v_pk_add_f32 v[4:5], v[100:101], v[100:101]
	s_waitcnt lgkmcnt(0)
	v_add_f32_e32 v14, v14, v15
	s_nop 1
	v_mov_b32_e32 v160, v14
	v_mov_b32_e32 v161, v14
	s_nop 1
	v_permlane16_swap_b32_e32 v160, v161
	s_nop 1
	v_permlane16_swap_b32_e32 v161, v160
	v_mov_b32_e32 v15, v161
	ds_write_b128 v122, v[2:5]
	v_pk_mul_f32 v[2:3], v[12:13], v[74:75] op_sel_hi:[1,0]
	v_pk_mul_f32 v[4:5], v[22:23], v[74:75] op_sel_hi:[1,0]
	v_pk_mul_f32 v[140:141], v[42:43], v[2:3]
	s_waitcnt lgkmcnt(1)
	v_add_f32_e32 v12, v14, v15
	s_nop 1
	v_mov_b32_e32 v160, v12
	v_mov_b32_e32 v161, v12
	s_nop 1
	v_permlane32_swap_b32_e32 v160, v161
	s_nop 1
	v_permlane32_swap_b32_e32 v161, v160
	v_mov_b32_e32 v13, v161
	v_pk_mul_f32 v[102:103], v[40:41], v[4:5]
	v_pk_add_f32 v[4:5], v[140:141], v[140:141]
	v_pk_add_f32 v[2:3], v[102:103], v[102:103]
	ds_write_b128 v123, v[2:5]
	s_waitcnt lgkmcnt(1)
	v_add_f32_e32 v4, v12, v13
	v_fmamk_f32 v4, v4, 0x3a800000, v119
	v_mul_f32_e32 v5, 0x4f800000, v4
	v_cmp_gt_f32_e32 vcc, s27, v4
	v_pk_mul_f32 v[2:3], v[10:11], v[74:75] op_sel_hi:[1,0]
	s_nop 0
	v_cndmask_b32_e32 v10, v4, v5, vcc
	v_sqrt_f32_e32 v11, v10
	v_pk_mul_f32 v[144:145], v[46:47], v[2:3]
	v_pk_mul_f32 v[4:5], v[24:25], v[74:75] op_sel_hi:[1,0]
	v_add_u32_e32 v2, -1, v11
	v_fma_f32 v3, -v2, v11, v10
	v_cmp_ge_f32_e64 s[14:15], 0, v3
	v_add_u32_e32 v3, 1, v11
	v_pk_mul_f32 v[142:143], v[44:45], v[4:5]
	v_fma_f32 v4, -v3, v11, v10
	v_cndmask_b32_e64 v2, v11, v2, s[14:15]
	v_cmp_lt_f32_e64 s[14:15], 0, v4
	v_pk_add_f32 v[4:5], v[144:145], v[144:145]
	s_nop 0
	v_cndmask_b32_e64 v2, v2, v3, s[14:15]
	v_mul_f32_e32 v3, 0x37800000, v2
	v_cndmask_b32_e32 v2, v2, v3, vcc
	v_cmp_class_f32_e32 vcc, v10, v120
	s_nop 1
	v_cndmask_b32_e32 v10, v2, v10, vcc
	v_div_scale_f32 v11, s[14:15], v10, v10, 1.0
	v_rcp_f32_e32 v12, v11
	v_pk_add_f32 v[2:3], v[142:143], v[142:143]
	ds_write_b128 v124, v[2:5]
	v_fma_f32 v2, -v11, v12, 1.0
	v_fmac_f32_e32 v12, v2, v12
	v_div_scale_f32 v2, vcc, 1.0, v10, 1.0
	v_mul_f32_e32 v3, v2, v12
	v_fma_f32 v4, -v11, v3, v2
	v_fmac_f32_e32 v3, v4, v12
	v_fma_f32 v2, -v11, v3, v2
	v_div_fmas_f32 v2, v2, v12, v3
	v_div_fixup_f32 v4, v2, v10, 1.0
	v_pk_mul_f32 v[2:3], v[8:9], v[4:5] op_sel_hi:[1,0]
	v_pk_mul_f32 v[0:1], v[0:1], v[4:5] op_sel_hi:[1,0]
	v_pk_mul_f32 v[74:75], v[34:35], v[2:3]
	v_pk_mul_f32 v[76:77], v[32:33], v[0:1]
	v_pk_add_f32 v[2:3], v[74:75], v[74:75]
	v_pk_add_f32 v[0:1], v[76:77], v[76:77]
	ds_write_b128 v125, v[0:3]
	v_pk_mul_f32 v[0:1], v[6:7], v[4:5] op_sel_hi:[1,0]
	v_pk_mul_f32 v[2:3], v[26:27], v[4:5] op_sel_hi:[1,0]
	v_pk_mul_f32 v[78:79], v[38:39], v[0:1]
	v_pk_mul_f32 v[80:81], v[36:37], v[2:3]
	v_pk_add_f32 v[2:3], v[78:79], v[78:79]
	v_pk_add_f32 v[0:1], v[80:81], v[80:81]
	ds_write_b128 v126, v[0:3]
	v_pk_mul_f32 v[0:1], v[30:31], v[4:5] op_sel_hi:[1,0]
	v_pk_mul_f32 v[2:3], v[28:29], v[4:5] op_sel_hi:[1,0]
	v_pk_mul_f32 v[82:83], v[42:43], v[0:1]
	v_pk_mul_f32 v[84:85], v[40:41], v[2:3]
	v_pk_add_f32 v[2:3], v[82:83], v[82:83]
	v_pk_add_f32 v[0:1], v[84:85], v[84:85]
	ds_write_b128 v127, v[0:3]
	v_pk_mul_f32 v[0:1], v[88:89], v[4:5] op_sel_hi:[1,0]
	v_pk_mul_f32 v[2:3], v[86:87], v[4:5] op_sel_hi:[1,0]
	v_pk_mul_f32 v[86:87], v[46:47], v[0:1]
	v_pk_mul_f32 v[88:89], v[44:45], v[2:3]
	v_pk_add_f32 v[2:3], v[86:87], v[86:87]
	v_pk_add_f32 v[0:1], v[88:89], v[88:89]
	ds_write_b128 v128, v[0:3]
	s_waitcnt lgkmcnt(0)
	ds_read_b128 v[0:3], v129
	ds_read_b128 v[4:7], v130
	ds_read_b128 v[8:11], v131
	ds_read_b128 v[12:15], v132
	ds_read_b128 v[28:31], v135
	ds_read_b128 v[90:93], v136
	s_waitcnt lgkmcnt(4)
	v_med3_f32 v16, v4, s38, v138
	v_med3_f32 v17, v5, s38, v138
	v_med3_f32 v18, v6, s38, v138
	v_med3_f32 v19, v7, s38, v138
	s_waitcnt lgkmcnt(3)
	v_med3_f32 v4, v8, s38, v138
	v_med3_f32 v5, v9, s38, v138
	v_med3_f32 v6, v10, s38, v138
	v_med3_f32 v7, v11, s38, v138
	s_waitcnt lgkmcnt(2)
	v_med3_f32 v20, v12, s38, v138
	ds_read_b128 v[8:11], v133
	v_med3_f32 v21, v13, s38, v138
	v_med3_f32 v22, v14, s38, v138
	v_med3_f32 v23, v15, s38, v138
	ds_read_b128 v[12:15], v134
	v_med3_f32 v0, v0, s38, v138
	v_med3_f32 v1, v1, s38, v138
	v_med3_f32 v2, v2, s38, v138
	v_med3_f32 v3, v3, s38, v138
	s_waitcnt lgkmcnt(1)
	v_med3_f32 v8, v8, s38, v138
	v_med3_f32 v9, v9, s38, v138
	v_med3_f32 v10, v10, s38, v138
	v_med3_f32 v11, v11, s38, v138
	s_waitcnt lgkmcnt(0)
	v_med3_f32 v24, v12, s38, v138
	v_med3_f32 v25, v13, s38, v138
	v_med3_f32 v26, v14, s38, v138
	v_med3_f32 v27, v15, s38, v138
	v_med3_f32 v12, v28, s38, v138
	v_med3_f32 v13, v29, s38, v138
	v_med3_f32 v14, v30, s38, v138
	v_med3_f32 v15, v31, s38, v138
	v_med3_f32 v28, v90, s38, v138
	v_med3_f32 v29, v91, s38, v138
	v_med3_f32 v30, v92, s38, v138
	v_med3_f32 v31, v93, s38, v138
	v_cvt_scalef32_2xpk16_fp6_f32 v[0:5], v[0:15], v[16:31], 1.0
	v_add_u32_e32 v8, s26, v110
	v_mov_b64_e32 v[6:7], s[20:21]
	v_mad_i64_i32 v[6:7], s[14:15], v8, s3, v[6:7]
	v_lshl_add_u64 v[8:9], v[6:7], 0, v[48:49]
	global_store_dwordx4 v[8:9], v[0:3], off
	v_mov_b32_e32 v8, v96
	v_mov_b32_e32 v9, v74
	v_lshl_add_u64 v[0:1], v[6:7], 0, v[50:51]
	global_store_dwordx2 v[0:1], v[4:5], off offset:512
	ds_read_b128 v[0:3], v111
	ds_read_b128 v[22:25], v111 offset:1024
	v_mov_b32_e32 v6, v94
	v_mov_b32_e32 v7, v76
	v_mov_b32_e32 v76, v95
	s_waitcnt lgkmcnt(1)
	v_pk_fma_f32 v[4:5], v[6:7], v[0:1], 0 op_sel_hi:[1,0,0]
	v_mov_b32_e32 v74, v97
	v_pk_fma_f32 v[0:1], v[76:77], v[0:1], v[4:5] op_sel:[0,1,0]
	v_mov_b32_e32 v12, v98
	v_pk_fma_f32 v[0:1], v[8:9], v[2:3], v[0:1] op_sel_hi:[1,0,1]
	v_mov_b32_e32 v2, v3
	v_mov_b32_e32 v13, v80
	v_pk_fma_f32 v[0:1], v[74:75], v[2:3], v[0:1] op_sel_hi:[1,0,1]
	v_mov_b32_e32 v80, v99
	s_waitcnt lgkmcnt(0)
	v_pk_fma_f32 v[0:1], v[12:13], v[22:23], v[0:1] op_sel_hi:[1,0,1]
	v_mov_b32_e32 v16, v100
	v_pk_fma_f32 v[4:5], v[80:81], v[22:23], v[0:1] op_sel:[0,1,0]
	ds_read_b128 v[0:3], v111 offset:2048
	v_mov_b32_e32 v17, v78
	v_mov_b32_e32 v78, v101
	v_pk_fma_f32 v[4:5], v[16:17], v[24:25], v[4:5] op_sel_hi:[1,0,1]
	v_mov_b32_e32 v22, v25
	v_mov_b32_e32 v10, v102
	v_mov_b32_e32 v11, v84
	v_pk_fma_f32 v[4:5], v[78:79], v[22:23], v[4:5] op_sel_hi:[1,0,1]
	ds_read_b128 v[22:25], v111 offset:3072
	v_mov_b32_e32 v84, v103
	s_waitcnt lgkmcnt(1)
	v_pk_fma_f32 v[4:5], v[10:11], v[0:1], v[4:5] op_sel_hi:[1,0,1]
	v_mov_b32_e32 v14, v140
	v_mov_b32_e32 v15, v82
	v_pk_fma_f32 v[0:1], v[84:85], v[0:1], v[4:5] op_sel:[0,1,0]
	v_mov_b32_e32 v82, v141
	v_pk_fma_f32 v[0:1], v[14:15], v[2:3], v[0:1] op_sel_hi:[1,0,1]
	v_mov_b32_e32 v2, v3
	v_mov_b32_e32 v18, v142
	v_mov_b32_e32 v19, v88
	v_pk_fma_f32 v[0:1], v[82:83], v[2:3], v[0:1] op_sel_hi:[1,0,1]
	v_mov_b32_e32 v88, v143
	s_waitcnt lgkmcnt(0)
	v_pk_fma_f32 v[0:1], v[18:19], v[22:23], v[0:1] op_sel_hi:[1,0,1]
	v_mov_b32_e32 v20, v144
	v_mov_b32_e32 v21, v86
	v_pk_fma_f32 v[0:1], v[88:89], v[22:23], v[0:1] op_sel:[0,1,0]
	v_mov_b32_e32 v86, v145
	v_pk_fma_f32 v[0:1], v[20:21], v[24:25], v[0:1] op_sel_hi:[1,0,1]
	v_mov_b32_e32 v2, v25
	v_pk_fma_f32 v[0:1], v[86:87], v[2:3], v[0:1] op_sel_hi:[1,0,1]
	s_nop 0
	ds_read_b128 v[2:5], v111 offset:4096
	ds_read_b128 v[22:25], v111 offset:5120
	ds_read_b128 v[26:29], v111 offset:6144
	s_waitcnt lgkmcnt(2)
	v_pk_fma_f32 v[30:31], v[6:7], v[2:3], 0 op_sel_hi:[1,0,0]
	s_nop 0
	v_pk_fma_f32 v[2:3], v[76:77], v[2:3], v[30:31] op_sel:[0,1,0]
	v_mov_b32_e32 v90, v5
	v_pk_fma_f32 v[2:3], v[8:9], v[4:5], v[2:3] op_sel_hi:[1,0,1]
	s_waitcnt lgkmcnt(1)
	v_mov_b32_e32 v92, v25
	v_pk_fma_f32 v[2:3], v[74:75], v[90:91], v[2:3] op_sel_hi:[1,0,1]
	s_nop 0
	v_pk_fma_f32 v[2:3], v[12:13], v[22:23], v[2:3] op_sel_hi:[1,0,1]
	s_nop 0
	v_pk_fma_f32 v[2:3], v[80:81], v[22:23], v[2:3] op_sel:[0,1,0]
	s_nop 0
	v_pk_fma_f32 v[2:3], v[16:17], v[24:25], v[2:3] op_sel_hi:[1,0,1]
	s_waitcnt lgkmcnt(0)
	v_mov_b32_e32 v24, v29
	v_pk_fma_f32 v[22:23], v[78:79], v[92:93], v[2:3] op_sel_hi:[1,0,1]
	ds_read_b128 v[2:5], v111 offset:7168
	v_pk_fma_f32 v[22:23], v[10:11], v[26:27], v[22:23] op_sel_hi:[1,0,1]
	s_nop 0
	v_pk_fma_f32 v[22:23], v[84:85], v[26:27], v[22:23] op_sel:[0,1,0]
	s_nop 0
	v_pk_fma_f32 v[22:23], v[14:15], v[28:29], v[22:23] op_sel_hi:[1,0,1]
	s_nop 0
	v_pk_fma_f32 v[22:23], v[82:83], v[24:25], v[22:23] op_sel_hi:[1,0,1]
	s_waitcnt lgkmcnt(0)
	v_pk_fma_f32 v[22:23], v[18:19], v[2:3], v[22:23] op_sel_hi:[1,0,1]
	s_nop 0
	v_pk_fma_f32 v[2:3], v[88:89], v[2:3], v[22:23] op_sel:[0,1,0]
	s_nop 0
	v_pk_fma_f32 v[2:3], v[20:21], v[4:5], v[2:3] op_sel_hi:[1,0,1]
	v_mov_b32_e32 v4, v5
	v_pk_fma_f32 v[2:3], v[86:87], v[4:5], v[2:3] op_sel_hi:[1,0,1]
	s_nop 0
	ds_read_b128 v[22:25], v111 offset:8192
	ds_read_b128 v[26:29], v111 offset:9216
	ds_read_b128 v[90:93], v111 offset:10240
	s_waitcnt lgkmcnt(2)
	v_pk_fma_f32 v[4:5], v[6:7], v[22:23], 0 op_sel_hi:[1,0,0]
	s_nop 0
	v_pk_fma_f32 v[4:5], v[76:77], v[22:23], v[4:5] op_sel:[0,1,0]
	v_mov_b32_e32 v30, v25
	v_pk_fma_f32 v[4:5], v[8:9], v[24:25], v[4:5] op_sel_hi:[1,0,1]
	s_waitcnt lgkmcnt(1)
	v_mov_b32_e32 v94, v29
	v_pk_fma_f32 v[4:5], v[74:75], v[30:31], v[4:5] op_sel_hi:[1,0,1]
	ds_read_b128 v[22:25], v111 offset:11264
	v_pk_fma_f32 v[4:5], v[12:13], v[26:27], v[4:5] op_sel_hi:[1,0,1]
	s_nop 0
	v_pk_fma_f32 v[4:5], v[80:81], v[26:27], v[4:5] op_sel:[0,1,0]
	s_waitcnt lgkmcnt(1)
	v_mov_b32_e32 v26, v93
	v_pk_fma_f32 v[4:5], v[16:17], v[28:29], v[4:5] op_sel_hi:[1,0,1]
	s_nop 0
	v_pk_fma_f32 v[4:5], v[78:79], v[94:95], v[4:5] op_sel_hi:[1,0,1]
	s_nop 0
	v_pk_fma_f32 v[4:5], v[10:11], v[90:91], v[4:5] op_sel_hi:[1,0,1]
	s_nop 0
	v_pk_fma_f32 v[4:5], v[84:85], v[90:91], v[4:5] op_sel:[0,1,0]
	s_nop 0
	v_pk_fma_f32 v[4:5], v[14:15], v[92:93], v[4:5] op_sel_hi:[1,0,1]
	s_nop 0
	v_pk_fma_f32 v[4:5], v[82:83], v[26:27], v[4:5] op_sel_hi:[1,0,1]
	s_waitcnt lgkmcnt(0)
	v_pk_fma_f32 v[4:5], v[18:19], v[22:23], v[4:5] op_sel_hi:[1,0,1]
	s_nop 0
	v_pk_fma_f32 v[4:5], v[88:89], v[22:23], v[4:5] op_sel:[0,1,0]
	v_mov_b32_e32 v22, v25
	v_pk_fma_f32 v[4:5], v[20:21], v[24:25], v[4:5] op_sel_hi:[1,0,1]
	s_nop 0
	v_pk_fma_f32 v[4:5], v[86:87], v[22:23], v[4:5] op_sel_hi:[1,0,1]
	s_nop 0
	ds_read_b128 v[22:25], v111 offset:12288
	ds_read_b128 v[26:29], v111 offset:13312
	ds_read_b128 v[90:93], v111 offset:14336
	s_waitcnt lgkmcnt(2)
	v_pk_fma_f32 v[30:31], v[6:7], v[22:23], 0 op_sel_hi:[1,0,0]
	s_nop 0
	v_pk_fma_f32 v[22:23], v[76:77], v[22:23], v[30:31] op_sel:[0,1,0]
	v_mov_b32_e32 v94, v25
	v_pk_fma_f32 v[22:23], v[8:9], v[24:25], v[22:23] op_sel_hi:[1,0,1]
	s_waitcnt lgkmcnt(1)
	v_mov_b32_e32 v96, v29
	v_pk_fma_f32 v[22:23], v[74:75], v[94:95], v[22:23] op_sel_hi:[1,0,1]
	s_nop 0
	v_pk_fma_f32 v[22:23], v[12:13], v[26:27], v[22:23] op_sel_hi:[1,0,1]
	s_nop 0
	v_pk_fma_f32 v[22:23], v[80:81], v[26:27], v[22:23] op_sel:[0,1,0]
	s_nop 0
	v_pk_fma_f32 v[22:23], v[16:17], v[28:29], v[22:23] op_sel_hi:[1,0,1]
	s_waitcnt lgkmcnt(0)
	v_mov_b32_e32 v28, v93
	v_pk_fma_f32 v[26:27], v[78:79], v[96:97], v[22:23] op_sel_hi:[1,0,1]
	ds_read_b128 v[22:25], v111 offset:15360
	v_pk_fma_f32 v[26:27], v[10:11], v[90:91], v[26:27] op_sel_hi:[1,0,1]
	s_nop 0
	v_pk_fma_f32 v[26:27], v[84:85], v[90:91], v[26:27] op_sel:[0,1,0]
	s_nop 0
	v_pk_fma_f32 v[26:27], v[14:15], v[92:93], v[26:27] op_sel_hi:[1,0,1]
	s_nop 0
	v_pk_fma_f32 v[26:27], v[82:83], v[28:29], v[26:27] op_sel_hi:[1,0,1]
	s_waitcnt lgkmcnt(0)
	v_pk_fma_f32 v[26:27], v[18:19], v[22:23], v[26:27] op_sel_hi:[1,0,1]
	s_nop 0
	v_pk_fma_f32 v[22:23], v[88:89], v[22:23], v[26:27] op_sel:[0,1,0]
	s_nop 0
	v_pk_fma_f32 v[22:23], v[20:21], v[24:25], v[22:23] op_sel_hi:[1,0,1]
	v_mov_b32_e32 v24, v25
	v_pk_fma_f32 v[22:23], v[86:87], v[24:25], v[22:23] op_sel_hi:[1,0,1]
	s_nop 0
	ds_read_b128 v[24:27], v111 offset:16384
	ds_read_b128 v[28:31], v111 offset:17408
	ds_read_b128 v[90:93], v111 offset:18432
	s_waitcnt lgkmcnt(2)
	v_pk_fma_f32 v[94:95], v[6:7], v[24:25], 0 op_sel_hi:[1,0,0]
	s_nop 0
	v_pk_fma_f32 v[24:25], v[76:77], v[24:25], v[94:95] op_sel:[0,1,0]
	v_mov_b32_e32 v96, v27
	v_pk_fma_f32 v[24:25], v[8:9], v[26:27], v[24:25] op_sel_hi:[1,0,1]
	s_waitcnt lgkmcnt(1)
	v_mov_b32_e32 v98, v31
	v_pk_fma_f32 v[24:25], v[74:75], v[96:97], v[24:25] op_sel_hi:[1,0,1]
	s_nop 0
	v_pk_fma_f32 v[24:25], v[12:13], v[28:29], v[24:25] op_sel_hi:[1,0,1]
	s_nop 0
	v_pk_fma_f32 v[24:25], v[80:81], v[28:29], v[24:25] op_sel:[0,1,0]
	s_nop 0
	v_pk_fma_f32 v[24:25], v[16:17], v[30:31], v[24:25] op_sel_hi:[1,0,1]
	s_waitcnt lgkmcnt(0)
	v_mov_b32_e32 v30, v93
	v_pk_fma_f32 v[28:29], v[78:79], v[98:99], v[24:25] op_sel_hi:[1,0,1]
	ds_read_b128 v[24:27], v111 offset:19456
	v_pk_fma_f32 v[28:29], v[10:11], v[90:91], v[28:29] op_sel_hi:[1,0,1]
	s_nop 0
	v_pk_fma_f32 v[28:29], v[84:85], v[90:91], v[28:29] op_sel:[0,1,0]
	s_nop 0
	v_pk_fma_f32 v[28:29], v[14:15], v[92:93], v[28:29] op_sel_hi:[1,0,1]
	s_nop 0
	v_pk_fma_f32 v[28:29], v[82:83], v[30:31], v[28:29] op_sel_hi:[1,0,1]
	s_waitcnt lgkmcnt(0)
	v_pk_fma_f32 v[28:29], v[18:19], v[24:25], v[28:29] op_sel_hi:[1,0,1]
	s_nop 0
	v_pk_fma_f32 v[24:25], v[88:89], v[24:25], v[28:29] op_sel:[0,1,0]
	s_nop 0
	v_pk_fma_f32 v[24:25], v[20:21], v[26:27], v[24:25] op_sel_hi:[1,0,1]
	v_mov_b32_e32 v26, v27
	v_pk_fma_f32 v[24:25], v[86:87], v[26:27], v[24:25] op_sel_hi:[1,0,1]
	s_nop 0
	ds_read_b128 v[26:29], v111 offset:20480
	ds_read_b128 v[90:93], v111 offset:21504
	ds_read_b128 v[94:97], v111 offset:22528
	s_waitcnt lgkmcnt(2)
	v_pk_fma_f32 v[30:31], v[6:7], v[26:27], 0 op_sel_hi:[1,0,0]
	s_nop 0
	v_pk_fma_f32 v[26:27], v[76:77], v[26:27], v[30:31] op_sel:[0,1,0]
	v_mov_b32_e32 v98, v29
	v_pk_fma_f32 v[26:27], v[8:9], v[28:29], v[26:27] op_sel_hi:[1,0,1]
	s_waitcnt lgkmcnt(1)
	v_mov_b32_e32 v100, v93
	v_pk_fma_f32 v[26:27], v[74:75], v[98:99], v[26:27] op_sel_hi:[1,0,1]
	s_nop 0
	v_pk_fma_f32 v[26:27], v[12:13], v[90:91], v[26:27] op_sel_hi:[1,0,1]
	s_nop 0
	v_pk_fma_f32 v[26:27], v[80:81], v[90:91], v[26:27] op_sel:[0,1,0]
	s_waitcnt lgkmcnt(0)
	v_mov_b32_e32 v90, v97
	v_pk_fma_f32 v[26:27], v[16:17], v[92:93], v[26:27] op_sel_hi:[1,0,1]
	s_nop 0
	v_pk_fma_f32 v[30:31], v[78:79], v[100:101], v[26:27] op_sel_hi:[1,0,1]
	ds_read_b128 v[26:29], v111 offset:23552
	v_pk_fma_f32 v[30:31], v[10:11], v[94:95], v[30:31] op_sel_hi:[1,0,1]
	s_nop 0
	v_pk_fma_f32 v[30:31], v[84:85], v[94:95], v[30:31] op_sel:[0,1,0]
	s_nop 0
	v_pk_fma_f32 v[30:31], v[14:15], v[96:97], v[30:31] op_sel_hi:[1,0,1]
	s_nop 0
	v_pk_fma_f32 v[30:31], v[82:83], v[90:91], v[30:31] op_sel_hi:[1,0,1]
	s_waitcnt lgkmcnt(0)
	v_pk_fma_f32 v[30:31], v[18:19], v[26:27], v[30:31] op_sel_hi:[1,0,1]
	s_nop 0
	v_pk_fma_f32 v[26:27], v[88:89], v[26:27], v[30:31] op_sel:[0,1,0]
	s_nop 0
	v_pk_fma_f32 v[26:27], v[20:21], v[28:29], v[26:27] op_sel_hi:[1,0,1]
	v_mov_b32_e32 v28, v29
	v_pk_fma_f32 v[26:27], v[86:87], v[28:29], v[26:27] op_sel_hi:[1,0,1]
	s_nop 0
	ds_read_b128 v[28:31], v111 offset:24576
	ds_read_b128 v[90:93], v111 offset:25600
	ds_read_b128 v[94:97], v111 offset:26624
	s_waitcnt lgkmcnt(2)
	v_pk_fma_f32 v[98:99], v[6:7], v[28:29], 0 op_sel_hi:[1,0,0]
	s_nop 0
	v_pk_fma_f32 v[28:29], v[76:77], v[28:29], v[98:99] op_sel:[0,1,0]
	v_mov_b32_e32 v100, v31
	v_pk_fma_f32 v[28:29], v[8:9], v[30:31], v[28:29] op_sel_hi:[1,0,1]
	s_waitcnt lgkmcnt(1)
	v_mov_b32_e32 v102, v93
	v_pk_fma_f32 v[28:29], v[74:75], v[100:101], v[28:29] op_sel_hi:[1,0,1]
	s_nop 0
	v_pk_fma_f32 v[28:29], v[12:13], v[90:91], v[28:29] op_sel_hi:[1,0,1]
	s_nop 0
	v_pk_fma_f32 v[28:29], v[80:81], v[90:91], v[28:29] op_sel:[0,1,0]
	s_nop 0
	v_pk_fma_f32 v[28:29], v[16:17], v[92:93], v[28:29] op_sel_hi:[1,0,1]
	s_waitcnt lgkmcnt(0)
	v_mov_b32_e32 v92, v97
	v_pk_fma_f32 v[90:91], v[78:79], v[102:103], v[28:29] op_sel_hi:[1,0,1]
	ds_read_b128 v[28:31], v111 offset:27648
	v_pk_fma_f32 v[90:91], v[10:11], v[94:95], v[90:91] op_sel_hi:[1,0,1]
	s_nop 0
	v_pk_fma_f32 v[90:91], v[84:85], v[94:95], v[90:91] op_sel:[0,1,0]
	s_nop 0
	v_pk_fma_f32 v[90:91], v[14:15], v[96:97], v[90:91] op_sel_hi:[1,0,1]
	s_nop 0
	v_pk_fma_f32 v[90:91], v[82:83], v[92:93], v[90:91] op_sel_hi:[1,0,1]
	s_waitcnt lgkmcnt(0)
	v_pk_fma_f32 v[90:91], v[18:19], v[28:29], v[90:91] op_sel_hi:[1,0,1]
	s_nop 0
	v_pk_fma_f32 v[28:29], v[88:89], v[28:29], v[90:91] op_sel:[0,1,0]
	s_nop 0
	v_pk_fma_f32 v[28:29], v[20:21], v[30:31], v[28:29] op_sel_hi:[1,0,1]
	v_mov_b32_e32 v30, v31
	v_pk_fma_f32 v[28:29], v[86:87], v[30:31], v[28:29] op_sel_hi:[1,0,1]
	s_nop 0
	ds_read_b128 v[90:93], v111 offset:28672
	ds_read_b128 v[94:97], v111 offset:29696
	ds_read_b128 v[98:101], v111 offset:30720
	s_waitcnt lgkmcnt(2)
	v_pk_fma_f32 v[30:31], v[6:7], v[90:91], 0 op_sel_hi:[1,0,0]
	s_nop 0
	v_pk_fma_f32 v[30:31], v[76:77], v[90:91], v[30:31] op_sel:[0,1,0]
	v_mov_b32_e32 v102, v93
	v_pk_fma_f32 v[30:31], v[8:9], v[92:93], v[30:31] op_sel_hi:[1,0,1]
	s_waitcnt lgkmcnt(1)
	v_mov_b32_e32 v140, v97
	v_pk_fma_f32 v[30:31], v[74:75], v[102:103], v[30:31] op_sel_hi:[1,0,1]
	ds_read_b128 v[90:93], v111 offset:31744
	v_pk_fma_f32 v[30:31], v[12:13], v[94:95], v[30:31] op_sel_hi:[1,0,1]
	s_nop 0
	v_pk_fma_f32 v[30:31], v[80:81], v[94:95], v[30:31] op_sel:[0,1,0]
	s_waitcnt lgkmcnt(1)
	v_mov_b32_e32 v94, v101
	v_pk_fma_f32 v[30:31], v[16:17], v[96:97], v[30:31] op_sel_hi:[1,0,1]
	s_nop 0
	v_pk_fma_f32 v[30:31], v[78:79], v[140:141], v[30:31] op_sel_hi:[1,0,1]
	s_nop 0
	v_pk_fma_f32 v[30:31], v[10:11], v[98:99], v[30:31] op_sel_hi:[1,0,1]
	s_nop 0
	v_pk_fma_f32 v[30:31], v[84:85], v[98:99], v[30:31] op_sel:[0,1,0]
	s_nop 0
	v_pk_fma_f32 v[30:31], v[14:15], v[100:101], v[30:31] op_sel_hi:[1,0,1]
	s_nop 0
	v_pk_fma_f32 v[30:31], v[82:83], v[94:95], v[30:31] op_sel_hi:[1,0,1]
	s_waitcnt lgkmcnt(0)
	v_pk_fma_f32 v[30:31], v[18:19], v[90:91], v[30:31] op_sel_hi:[1,0,1]
	s_nop 0
	v_pk_fma_f32 v[30:31], v[88:89], v[90:91], v[30:31] op_sel:[0,1,0]
	v_mov_b32_e32 v90, v93
	v_pk_fma_f32 v[30:31], v[20:21], v[92:93], v[30:31] op_sel_hi:[1,0,1]
	s_nop 0
	v_pk_fma_f32 v[30:31], v[86:87], v[90:91], v[30:31] op_sel_hi:[1,0,1]
	s_nop 0
	ds_read_b128 v[90:93], v111 offset:32768
	ds_read_b128 v[94:97], v111 offset:33792
	ds_read_b128 v[98:101], v111 offset:34816
	s_waitcnt lgkmcnt(2)
	v_pk_fma_f32 v[102:103], v[6:7], v[90:91], 0 op_sel_hi:[1,0,0]
	s_nop 0
	v_pk_fma_f32 v[90:91], v[76:77], v[90:91], v[102:103] op_sel:[0,1,0]
	v_mov_b32_e32 v140, v93
	v_pk_fma_f32 v[90:91], v[8:9], v[92:93], v[90:91] op_sel_hi:[1,0,1]
	s_waitcnt lgkmcnt(1)
	v_mov_b32_e32 v142, v97
	v_pk_fma_f32 v[90:91], v[74:75], v[140:141], v[90:91] op_sel_hi:[1,0,1]
	s_nop 0
	v_pk_fma_f32 v[90:91], v[12:13], v[94:95], v[90:91] op_sel_hi:[1,0,1]
	s_nop 0
	v_pk_fma_f32 v[90:91], v[80:81], v[94:95], v[90:91] op_sel:[0,1,0]
	s_nop 0
	v_pk_fma_f32 v[90:91], v[16:17], v[96:97], v[90:91] op_sel_hi:[1,0,1]
	s_waitcnt lgkmcnt(0)
	v_mov_b32_e32 v96, v101
	v_pk_fma_f32 v[94:95], v[78:79], v[142:143], v[90:91] op_sel_hi:[1,0,1]
	ds_read_b128 v[90:93], v111 offset:35840
	v_pk_fma_f32 v[94:95], v[10:11], v[98:99], v[94:95] op_sel_hi:[1,0,1]
	s_nop 0
	v_pk_fma_f32 v[94:95], v[84:85], v[98:99], v[94:95] op_sel:[0,1,0]
	s_nop 0
	v_pk_fma_f32 v[94:95], v[14:15], v[100:101], v[94:95] op_sel_hi:[1,0,1]
	s_nop 0
	v_pk_fma_f32 v[94:95], v[82:83], v[96:97], v[94:95] op_sel_hi:[1,0,1]
	s_waitcnt lgkmcnt(0)
	v_pk_fma_f32 v[94:95], v[18:19], v[90:91], v[94:95] op_sel_hi:[1,0,1]
	s_nop 0
	v_pk_fma_f32 v[90:91], v[88:89], v[90:91], v[94:95] op_sel:[0,1,0]
	s_nop 0
	v_pk_fma_f32 v[90:91], v[20:21], v[92:93], v[90:91] op_sel_hi:[1,0,1]
	v_mov_b32_e32 v92, v93
	v_pk_fma_f32 v[90:91], v[86:87], v[92:93], v[90:91] op_sel_hi:[1,0,1]
	s_nop 0
	ds_read_b128 v[92:95], v111 offset:36864
	ds_read_b128 v[96:99], v111 offset:37888
	ds_read_b128 v[100:103], v111 offset:38912
	s_waitcnt lgkmcnt(2)
	v_pk_fma_f32 v[140:141], v[6:7], v[92:93], 0 op_sel_hi:[1,0,0]
	s_nop 0
	v_pk_fma_f32 v[92:93], v[76:77], v[92:93], v[140:141] op_sel:[0,1,0]
	v_mov_b32_e32 v142, v95
	v_pk_fma_f32 v[92:93], v[8:9], v[94:95], v[92:93] op_sel_hi:[1,0,1]
	s_waitcnt lgkmcnt(1)
	v_mov_b32_e32 v144, v99
	v_pk_fma_f32 v[92:93], v[74:75], v[142:143], v[92:93] op_sel_hi:[1,0,1]
	s_nop 0
	v_pk_fma_f32 v[92:93], v[12:13], v[96:97], v[92:93] op_sel_hi:[1,0,1]
	s_nop 0
	v_pk_fma_f32 v[92:93], v[80:81], v[96:97], v[92:93] op_sel:[0,1,0]
	s_nop 0
	v_pk_fma_f32 v[92:93], v[16:17], v[98:99], v[92:93] op_sel_hi:[1,0,1]
	s_waitcnt lgkmcnt(0)
	v_mov_b32_e32 v98, v103
	v_pk_fma_f32 v[96:97], v[78:79], v[144:145], v[92:93] op_sel_hi:[1,0,1]
	ds_read_b128 v[92:95], v111 offset:39936
	v_pk_fma_f32 v[96:97], v[10:11], v[100:101], v[96:97] op_sel_hi:[1,0,1]
	s_nop 0
	v_pk_fma_f32 v[96:97], v[84:85], v[100:101], v[96:97] op_sel:[0,1,0]
	s_nop 0
	v_pk_fma_f32 v[96:97], v[14:15], v[102:103], v[96:97] op_sel_hi:[1,0,1]
	s_nop 0
	v_pk_fma_f32 v[96:97], v[82:83], v[98:99], v[96:97] op_sel_hi:[1,0,1]
	s_waitcnt lgkmcnt(0)
	v_pk_fma_f32 v[96:97], v[18:19], v[92:93], v[96:97] op_sel_hi:[1,0,1]
	s_nop 0
	v_pk_fma_f32 v[92:93], v[88:89], v[92:93], v[96:97] op_sel:[0,1,0]
	s_nop 0
	v_pk_fma_f32 v[92:93], v[20:21], v[94:95], v[92:93] op_sel_hi:[1,0,1]
	v_mov_b32_e32 v94, v95
	v_pk_fma_f32 v[92:93], v[86:87], v[94:95], v[92:93] op_sel_hi:[1,0,1]
	s_nop 0
	ds_read_b128 v[94:97], v111 offset:40960
	ds_read_b128 v[98:101], v111 offset:41984
	ds_read_b128 v[140:143], v111 offset:43008
	s_waitcnt lgkmcnt(2)
	v_pk_fma_f32 v[102:103], v[6:7], v[94:95], 0 op_sel_hi:[1,0,0]
	s_nop 0
	v_pk_fma_f32 v[94:95], v[76:77], v[94:95], v[102:103] op_sel:[0,1,0]
	v_mov_b32_e32 v144, v97
	v_pk_fma_f32 v[94:95], v[8:9], v[96:97], v[94:95] op_sel_hi:[1,0,1]
	s_waitcnt lgkmcnt(1)
	v_mov_b32_e32 v146, v101
	v_pk_fma_f32 v[94:95], v[74:75], v[144:145], v[94:95] op_sel_hi:[1,0,1]
	s_nop 0
	v_pk_fma_f32 v[94:95], v[12:13], v[98:99], v[94:95] op_sel_hi:[1,0,1]
	s_nop 0
	v_pk_fma_f32 v[94:95], v[80:81], v[98:99], v[94:95] op_sel:[0,1,0]
	s_nop 0
	v_pk_fma_f32 v[94:95], v[16:17], v[100:101], v[94:95] op_sel_hi:[1,0,1]
	s_waitcnt lgkmcnt(0)
	v_mov_b32_e32 v100, v143
	v_pk_fma_f32 v[98:99], v[78:79], v[146:147], v[94:95] op_sel_hi:[1,0,1]
	ds_read_b128 v[94:97], v111 offset:44032
	v_pk_fma_f32 v[98:99], v[10:11], v[140:141], v[98:99] op_sel_hi:[1,0,1]
	s_nop 0
	v_pk_fma_f32 v[98:99], v[84:85], v[140:141], v[98:99] op_sel:[0,1,0]
	s_nop 0
	v_pk_fma_f32 v[98:99], v[14:15], v[142:143], v[98:99] op_sel_hi:[1,0,1]
	s_nop 0
	v_pk_fma_f32 v[98:99], v[82:83], v[100:101], v[98:99] op_sel_hi:[1,0,1]
	s_waitcnt lgkmcnt(0)
	v_pk_fma_f32 v[98:99], v[18:19], v[94:95], v[98:99] op_sel_hi:[1,0,1]
	s_nop 0
	v_pk_fma_f32 v[94:95], v[88:89], v[94:95], v[98:99] op_sel:[0,1,0]
	s_nop 0
	v_pk_fma_f32 v[94:95], v[20:21], v[96:97], v[94:95] op_sel_hi:[1,0,1]
	v_mov_b32_e32 v96, v97
	v_pk_fma_f32 v[94:95], v[86:87], v[96:97], v[94:95] op_sel_hi:[1,0,1]
	s_nop 0
	ds_read_b128 v[96:99], v111 offset:45056
	ds_read_b128 v[100:103], v111 offset:46080
	ds_read_b128 v[140:143], v111 offset:47104
	s_waitcnt lgkmcnt(2)
	v_pk_fma_f32 v[144:145], v[6:7], v[96:97], 0 op_sel_hi:[1,0,0]
	s_nop 0
	v_pk_fma_f32 v[96:97], v[76:77], v[96:97], v[144:145] op_sel:[0,1,0]
	v_mov_b32_e32 v146, v99
	v_pk_fma_f32 v[96:97], v[8:9], v[98:99], v[96:97] op_sel_hi:[1,0,1]
	s_waitcnt lgkmcnt(1)
	v_mov_b32_e32 v148, v103
	v_pk_fma_f32 v[96:97], v[74:75], v[146:147], v[96:97] op_sel_hi:[1,0,1]
	s_nop 0
	v_pk_fma_f32 v[96:97], v[12:13], v[100:101], v[96:97] op_sel_hi:[1,0,1]
	s_nop 0
	v_pk_fma_f32 v[96:97], v[80:81], v[100:101], v[96:97] op_sel:[0,1,0]
	s_nop 0
	v_pk_fma_f32 v[96:97], v[16:17], v[102:103], v[96:97] op_sel_hi:[1,0,1]
	s_waitcnt lgkmcnt(0)
	v_mov_b32_e32 v102, v143
	v_pk_fma_f32 v[100:101], v[78:79], v[148:149], v[96:97] op_sel_hi:[1,0,1]
	ds_read_b128 v[96:99], v111 offset:48128
	v_pk_fma_f32 v[100:101], v[10:11], v[140:141], v[100:101] op_sel_hi:[1,0,1]
	s_nop 0
	v_pk_fma_f32 v[100:101], v[84:85], v[140:141], v[100:101] op_sel:[0,1,0]
	s_nop 0
	v_pk_fma_f32 v[100:101], v[14:15], v[142:143], v[100:101] op_sel_hi:[1,0,1]
	s_nop 0
	v_pk_fma_f32 v[100:101], v[82:83], v[102:103], v[100:101] op_sel_hi:[1,0,1]
	s_waitcnt lgkmcnt(0)
	v_pk_fma_f32 v[100:101], v[18:19], v[96:97], v[100:101] op_sel_hi:[1,0,1]
	s_nop 0
	v_pk_fma_f32 v[96:97], v[88:89], v[96:97], v[100:101] op_sel:[0,1,0]
	s_nop 0
	v_pk_fma_f32 v[96:97], v[20:21], v[98:99], v[96:97] op_sel_hi:[1,0,1]
	v_mov_b32_e32 v98, v99
	v_pk_fma_f32 v[96:97], v[86:87], v[98:99], v[96:97] op_sel_hi:[1,0,1]
	s_nop 0
	ds_read_b128 v[98:101], v111 offset:49152
	ds_read_b128 v[140:143], v111 offset:50176
	ds_read_b128 v[144:147], v111 offset:51200
	s_waitcnt lgkmcnt(2)
	v_pk_fma_f32 v[102:103], v[6:7], v[98:99], 0 op_sel_hi:[1,0,0]
	s_nop 0
	v_pk_fma_f32 v[98:99], v[76:77], v[98:99], v[102:103] op_sel:[0,1,0]
	v_mov_b32_e32 v148, v101
	v_pk_fma_f32 v[98:99], v[8:9], v[100:101], v[98:99] op_sel_hi:[1,0,1]
	s_waitcnt lgkmcnt(1)
	v_mov_b32_e32 v150, v143
	v_pk_fma_f32 v[98:99], v[74:75], v[148:149], v[98:99] op_sel_hi:[1,0,1]
	s_nop 0
	v_pk_fma_f32 v[98:99], v[12:13], v[140:141], v[98:99] op_sel_hi:[1,0,1]
	s_nop 0
	v_pk_fma_f32 v[98:99], v[80:81], v[140:141], v[98:99] op_sel:[0,1,0]
	s_waitcnt lgkmcnt(0)
	v_mov_b32_e32 v140, v147
	v_pk_fma_f32 v[98:99], v[16:17], v[142:143], v[98:99] op_sel_hi:[1,0,1]
	s_nop 0
	v_pk_fma_f32 v[102:103], v[78:79], v[150:151], v[98:99] op_sel_hi:[1,0,1]
	ds_read_b128 v[98:101], v111 offset:52224
	v_pk_fma_f32 v[102:103], v[10:11], v[144:145], v[102:103] op_sel_hi:[1,0,1]
	s_nop 0
	v_pk_fma_f32 v[102:103], v[84:85], v[144:145], v[102:103] op_sel:[0,1,0]
	s_nop 0
	v_pk_fma_f32 v[102:103], v[14:15], v[146:147], v[102:103] op_sel_hi:[1,0,1]
	s_nop 0
	v_pk_fma_f32 v[102:103], v[82:83], v[140:141], v[102:103] op_sel_hi:[1,0,1]
	s_waitcnt lgkmcnt(0)
	v_pk_fma_f32 v[102:103], v[18:19], v[98:99], v[102:103] op_sel_hi:[1,0,1]
	s_nop 0
	v_pk_fma_f32 v[98:99], v[88:89], v[98:99], v[102:103] op_sel:[0,1,0]
	s_nop 0
	v_pk_fma_f32 v[98:99], v[20:21], v[100:101], v[98:99] op_sel_hi:[1,0,1]
	v_mov_b32_e32 v100, v101
	v_pk_fma_f32 v[98:99], v[86:87], v[100:101], v[98:99] op_sel_hi:[1,0,1]
	s_nop 0
	ds_read_b128 v[100:103], v111 offset:53248
	ds_read_b128 v[140:143], v111 offset:54272
	ds_read_b128 v[144:147], v111 offset:55296
	s_waitcnt lgkmcnt(2)
	v_pk_fma_f32 v[148:149], v[6:7], v[100:101], 0 op_sel_hi:[1,0,0]
	s_nop 0
	v_pk_fma_f32 v[100:101], v[76:77], v[100:101], v[148:149] op_sel:[0,1,0]
	v_mov_b32_e32 v150, v103
	v_pk_fma_f32 v[100:101], v[8:9], v[102:103], v[100:101] op_sel_hi:[1,0,1]
	s_waitcnt lgkmcnt(1)
	v_mov_b32_e32 v152, v143
	v_pk_fma_f32 v[100:101], v[74:75], v[150:151], v[100:101] op_sel_hi:[1,0,1]
	s_nop 0
	v_pk_fma_f32 v[100:101], v[12:13], v[140:141], v[100:101] op_sel_hi:[1,0,1]
	s_nop 0
	v_pk_fma_f32 v[100:101], v[80:81], v[140:141], v[100:101] op_sel:[0,1,0]
	s_nop 0
	v_pk_fma_f32 v[100:101], v[16:17], v[142:143], v[100:101] op_sel_hi:[1,0,1]
	s_waitcnt lgkmcnt(0)
	v_mov_b32_e32 v142, v147
	v_pk_fma_f32 v[140:141], v[78:79], v[152:153], v[100:101] op_sel_hi:[1,0,1]
	ds_read_b128 v[100:103], v111 offset:56320
	v_pk_fma_f32 v[140:141], v[10:11], v[144:145], v[140:141] op_sel_hi:[1,0,1]
	s_nop 0
	v_pk_fma_f32 v[140:141], v[84:85], v[144:145], v[140:141] op_sel:[0,1,0]
	s_nop 0
	v_pk_fma_f32 v[140:141], v[14:15], v[146:147], v[140:141] op_sel_hi:[1,0,1]
	s_nop 0
	v_pk_fma_f32 v[140:141], v[82:83], v[142:143], v[140:141] op_sel_hi:[1,0,1]
	s_waitcnt lgkmcnt(0)
	v_pk_fma_f32 v[140:141], v[18:19], v[100:101], v[140:141] op_sel_hi:[1,0,1]
	s_nop 0
	v_pk_fma_f32 v[100:101], v[88:89], v[100:101], v[140:141] op_sel:[0,1,0]
	s_nop 0
	v_pk_fma_f32 v[100:101], v[20:21], v[102:103], v[100:101] op_sel_hi:[1,0,1]
	v_mov_b32_e32 v102, v103
	v_pk_fma_f32 v[100:101], v[86:87], v[102:103], v[100:101] op_sel_hi:[1,0,1]
	s_nop 0
	ds_read_b128 v[140:143], v111 offset:57344
	ds_read_b128 v[144:147], v111 offset:58368
	ds_read_b128 v[148:151], v111 offset:59392
	s_waitcnt lgkmcnt(2)
	v_pk_fma_f32 v[102:103], v[6:7], v[140:141], 0 op_sel_hi:[1,0,0]
	s_nop 0
	v_pk_fma_f32 v[102:103], v[76:77], v[140:141], v[102:103] op_sel:[0,1,0]
	v_mov_b32_e32 v152, v143
	v_pk_fma_f32 v[102:103], v[8:9], v[142:143], v[102:103] op_sel_hi:[1,0,1]
	s_waitcnt lgkmcnt(1)
	v_mov_b32_e32 v154, v147
	v_pk_fma_f32 v[102:103], v[74:75], v[152:153], v[102:103] op_sel_hi:[1,0,1]
	ds_read_b128 v[140:143], v111 offset:60416
	v_pk_fma_f32 v[102:103], v[12:13], v[144:145], v[102:103] op_sel_hi:[1,0,1]
	s_nop 0
	v_pk_fma_f32 v[102:103], v[80:81], v[144:145], v[102:103] op_sel:[0,1,0]
	s_waitcnt lgkmcnt(1)
	v_mov_b32_e32 v144, v151
	v_pk_fma_f32 v[102:103], v[16:17], v[146:147], v[102:103] op_sel_hi:[1,0,1]
	s_nop 0
	v_pk_fma_f32 v[102:103], v[78:79], v[154:155], v[102:103] op_sel_hi:[1,0,1]
	s_nop 0
	v_pk_fma_f32 v[102:103], v[10:11], v[148:149], v[102:103] op_sel_hi:[1,0,1]
	s_nop 0
	v_pk_fma_f32 v[102:103], v[84:85], v[148:149], v[102:103] op_sel:[0,1,0]
	s_nop 0
	v_pk_fma_f32 v[102:103], v[14:15], v[150:151], v[102:103] op_sel_hi:[1,0,1]
	s_nop 0
	v_pk_fma_f32 v[102:103], v[82:83], v[144:145], v[102:103] op_sel_hi:[1,0,1]
	s_waitcnt lgkmcnt(0)
	v_pk_fma_f32 v[102:103], v[18:19], v[140:141], v[102:103] op_sel_hi:[1,0,1]
	s_nop 0
	v_pk_fma_f32 v[102:103], v[88:89], v[140:141], v[102:103] op_sel:[0,1,0]
	v_mov_b32_e32 v140, v143
	v_pk_fma_f32 v[102:103], v[20:21], v[142:143], v[102:103] op_sel_hi:[1,0,1]
	s_nop 0
	v_pk_fma_f32 v[102:103], v[86:87], v[140:141], v[102:103] op_sel_hi:[1,0,1]
	s_nop 0
	ds_read_b128 v[140:143], v111 offset:61440
	ds_read_b128 v[144:147], v111 offset:62464
	ds_read_b128 v[148:151], v111 offset:63488
	s_waitcnt lgkmcnt(2)
	v_pk_fma_f32 v[6:7], v[6:7], v[140:141], 0 op_sel_hi:[1,0,0]
	s_nop 0
	v_pk_fma_f32 v[6:7], v[76:77], v[140:141], v[6:7] op_sel:[0,1,0]
	v_mov_b32_e32 v152, v143
	v_pk_fma_f32 v[6:7], v[8:9], v[142:143], v[6:7] op_sel_hi:[1,0,1]
	s_waitcnt lgkmcnt(1)
	v_mov_b32_e32 v154, v147
	v_pk_fma_f32 v[6:7], v[74:75], v[152:153], v[6:7] op_sel_hi:[1,0,1]
	s_nop 0
	v_pk_fma_f32 v[6:7], v[12:13], v[144:145], v[6:7] op_sel_hi:[1,0,1]
	s_nop 0
	v_pk_fma_f32 v[6:7], v[80:81], v[144:145], v[6:7] op_sel:[0,1,0]
	s_nop 0
	v_pk_fma_f32 v[6:7], v[16:17], v[146:147], v[6:7] op_sel_hi:[1,0,1]
	s_nop 0
	v_pk_fma_f32 v[12:13], v[78:79], v[154:155], v[6:7] op_sel_hi:[1,0,1]
	ds_read_b128 v[6:9], v111 offset:64512
	s_waitcnt lgkmcnt(1)
	v_pk_fma_f32 v[10:11], v[10:11], v[148:149], v[12:13] op_sel_hi:[1,0,1]
	v_mov_b32_e32 v12, v151
	v_pk_fma_f32 v[10:11], v[84:85], v[148:149], v[10:11] op_sel:[0,1,0]
	s_nop 0
	v_pk_fma_f32 v[10:11], v[14:15], v[150:151], v[10:11] op_sel_hi:[1,0,1]
	s_nop 0
	v_pk_fma_f32 v[10:11], v[82:83], v[12:13], v[10:11] op_sel_hi:[1,0,1]
	s_waitcnt lgkmcnt(0)
	v_pk_fma_f32 v[10:11], v[18:19], v[6:7], v[10:11] op_sel_hi:[1,0,1]
	s_nop 0
	v_pk_fma_f32 v[6:7], v[88:89], v[6:7], v[10:11] op_sel:[0,1,0]
	s_nop 0
	v_pk_fma_f32 v[6:7], v[20:21], v[8:9], v[6:7] op_sel_hi:[1,0,1]
	v_mov_b32_e32 v8, v9
	v_pk_fma_f32 v[6:7], v[86:87], v[8:9], v[6:7] op_sel_hi:[1,0,1]
	s_nop 0
	v_cndmask_b32_e64 v9, v2, v92, s[0:1]
	s_nop 1
	v_mov_b32_e32 v160, v9
	v_mov_b32_e32 v161, v9
	s_nop 1
	v_permlane32_swap_b32_e32 v160, v161
	s_nop 1
	v_permlane32_swap_b32_e32 v161, v160
	v_mov_b32_e32 v9, v161
	v_cndmask_b32_e64 v10, v4, v94, s[0:1]
	s_nop 1
	v_mov_b32_e32 v160, v10
	v_mov_b32_e32 v161, v10
	s_nop 1
	v_permlane32_swap_b32_e32 v160, v161
	s_nop 1
	v_permlane32_swap_b32_e32 v161, v160
	v_mov_b32_e32 v10, v161
	v_cndmask_b32_e64 v8, v90, v0, s[0:1]
	v_cndmask_b32_e64 v0, v0, v90, s[0:1]
	v_cndmask_b32_e64 v2, v92, v2, s[0:1]
	s_nop 1
	v_mov_b32_e32 v160, v0
	v_mov_b32_e32 v161, v0
	s_nop 1
	v_permlane32_swap_b32_e32 v160, v161
	s_nop 1
	v_permlane32_swap_b32_e32 v161, v160
	v_mov_b32_e32 v0, v161
	s_waitcnt lgkmcnt(2)
	v_add_f32_e32 v2, v2, v9
	v_cndmask_b32_e64 v4, v94, v4, s[0:1]
	v_cndmask_b32_e64 v9, v22, v96, s[0:1]
	s_waitcnt lgkmcnt(1)
	v_add_f32_e32 v4, v4, v10
	s_nop 1
	v_mov_b32_e32 v160, v9
	v_mov_b32_e32 v161, v9
	s_nop 1
	v_permlane32_swap_b32_e32 v160, v161
	s_nop 1
	v_permlane32_swap_b32_e32 v161, v160
	v_mov_b32_e32 v9, v161
	v_cndmask_b32_e64 v10, v24, v98, s[0:1]
	s_nop 1
	v_mov_b32_e32 v160, v10
	v_mov_b32_e32 v161, v10
	s_nop 1
	v_permlane32_swap_b32_e32 v160, v161
	s_nop 1
	v_permlane32_swap_b32_e32 v161, v160
	v_mov_b32_e32 v10, v161
	v_cndmask_b32_e64 v11, v26, v100, s[0:1]
	s_nop 1
	v_mov_b32_e32 v160, v11
	v_mov_b32_e32 v161, v11
	s_nop 1
	v_permlane32_swap_b32_e32 v160, v161
	s_nop 1
	v_permlane32_swap_b32_e32 v161, v160
	v_mov_b32_e32 v11, v161
	v_cndmask_b32_e64 v12, v28, v102, s[0:1]
	v_cndmask_b32_e64 v13, v30, v6, s[0:1]
	s_nop 1
	v_mov_b32_e32 v160, v12
	v_mov_b32_e32 v161, v12
	s_nop 1
	v_permlane32_swap_b32_e32 v160, v161
	s_nop 1
	v_permlane32_swap_b32_e32 v161, v160
	v_mov_b32_e32 v12, v161
	s_nop 1
	v_mov_b32_e32 v160, v13
	v_mov_b32_e32 v161, v13
	s_nop 1
	v_permlane32_swap_b32_e32 v160, v161
	s_nop 1
	v_permlane32_swap_b32_e32 v161, v160
	v_mov_b32_e32 v13, v161
	s_waitcnt lgkmcnt(5)
	v_add_f32_e32 v0, v8, v0
	v_cndmask_b32_e64 v8, v96, v22, s[0:1]
	s_waitcnt lgkmcnt(4)
	v_add_f32_e32 v8, v8, v9
	v_cndmask_b32_e64 v9, v98, v24, s[0:1]
	s_waitcnt lgkmcnt(3)
	v_add_f32_e32 v9, v9, v10
	v_cndmask_b32_e64 v10, v100, v26, s[0:1]
	s_waitcnt lgkmcnt(2)
	v_add_f32_e32 v10, v10, v11
	v_cndmask_b32_e64 v11, v102, v28, s[0:1]
	v_cndmask_b32_e64 v6, v6, v30, s[0:1]
	s_waitcnt lgkmcnt(1)
	v_add_f32_e32 v11, v11, v12
	s_waitcnt lgkmcnt(0)
	v_add_f32_e32 v6, v6, v13
	v_cndmask_b32_e64 v14, v0, v9, s[12:13]
	v_cndmask_b32_e64 v0, v9, v0, s[12:13]
	v_cndmask_b32_e64 v9, v10, v2, s[12:13]
	v_cndmask_b32_e64 v2, v2, v10, s[12:13]
	v_cndmask_b32_e64 v10, v4, v11, s[12:13]
	v_cndmask_b32_e64 v12, v8, v6, s[12:13]
	s_nop 1
	v_mov_b32_e32 v160, v14
	v_mov_b32_e32 v161, v14
	s_nop 1
	v_permlane16_swap_b32_e32 v160, v161
	s_nop 1
	v_permlane16_swap_b32_e32 v161, v160
	v_mov_b32_e32 v14, v161
	s_nop 1
	v_mov_b32_e32 v160, v2
	v_mov_b32_e32 v161, v2
	s_nop 1
	v_permlane16_swap_b32_e32 v160, v161
	s_nop 1
	v_permlane16_swap_b32_e32 v161, v160
	v_mov_b32_e32 v2, v161
	s_nop 1
	v_mov_b32_e32 v160, v10
	v_mov_b32_e32 v161, v10
	s_nop 1
	v_permlane16_swap_b32_e32 v160, v161
	s_nop 1
	v_permlane16_swap_b32_e32 v161, v160
	v_mov_b32_e32 v10, v161
	s_nop 1
	v_mov_b32_e32 v160, v12
	v_mov_b32_e32 v161, v12
	s_nop 1
	v_permlane16_swap_b32_e32 v160, v161
	s_nop 1
	v_permlane16_swap_b32_e32 v161, v160
	v_mov_b32_e32 v12, v161
	v_cndmask_b32_e64 v4, v11, v4, s[12:13]
	v_cndmask_b32_e64 v6, v6, v8, s[12:13]
	s_waitcnt lgkmcnt(3)
	v_add_f32_e32 v0, v0, v14
	s_waitcnt lgkmcnt(2)
	v_add_f32_e32 v2, v9, v2
	s_waitcnt lgkmcnt(1)
	v_add_f32_e32 v4, v4, v10
	s_waitcnt lgkmcnt(0)
	v_add_f32_e32 v6, v6, v12
	v_cndmask_b32_e64 v8, v0, v4, s[4:5]
	v_cndmask_b32_e64 v9, v2, v6, s[4:5]
	s_nop 1
	v_mov_b32_dpp v8, v8 row_ror:8 row_mask:0xf bank_mask:0xf
	s_nop 1
	v_mov_b32_dpp v9, v9 row_ror:8 row_mask:0xf bank_mask:0xf
	v_cndmask_b32_e64 v0, v4, v0, s[4:5]
	v_cndmask_b32_e64 v2, v6, v2, s[4:5]
	s_waitcnt lgkmcnt(1)
	v_add_f32_e32 v0, v0, v8
	s_waitcnt lgkmcnt(0)
	v_add_f32_e32 v2, v2, v9
	v_cndmask_b32_e64 v4, v0, v2, s[6:7]
	s_nop 1
	v_mov_b32_dpp v160, v4 row_half_mirror row_mask:0xf bank_mask:0xf
	s_nop 1
	v_mov_b32_dpp v4, v160 quad_perm:[3,2,1,0] row_mask:0xf bank_mask:0xf
	v_cndmask_b32_e64 v0, v2, v0, s[6:7]
	s_waitcnt lgkmcnt(0)
	v_add_f32_e32 v0, v0, v4
	s_nop 1
	v_mov_b32_dpp v2, v0 quad_perm:[2,3,0,1] row_mask:0xf bank_mask:0xf
	s_waitcnt lgkmcnt(0)
	v_add_f32_e32 v0, v0, v2
	s_nop 1
	v_mov_b32_dpp v2, v0 quad_perm:[1,0,3,2] row_mask:0xf bank_mask:0xf
	s_waitcnt lgkmcnt(0)
	v_add_f32_e32 v0, v0, v2
	s_nop 1
	v_mov_b32_dpp v160, v0 row_half_mirror row_mask:0xf bank_mask:0xf
	s_nop 1
	v_mov_b32_dpp v2, v160 quad_perm:[3,2,1,0] row_mask:0xf bank_mask:0xf
	s_waitcnt lgkmcnt(0)
	v_max_f32_e32 v2, v2, v2
	v_max_f32_e32 v2, v0, v2
	s_nop 1
	v_mov_b32_dpp v4, v2 row_ror:8 row_mask:0xf bank_mask:0xf
	s_waitcnt lgkmcnt(0)
	v_max_f32_e32 v4, v4, v4
	v_max_f32_e32 v2, v2, v4
	s_nop 1
	v_mov_b32_e32 v160, v2
	v_mov_b32_e32 v161, v2
	s_nop 1
	v_permlane16_swap_b32_e32 v160, v161
	s_nop 1
	v_permlane16_swap_b32_e32 v161, v160
	v_mov_b32_e32 v4, v161
	s_waitcnt lgkmcnt(0)
	v_max_f32_e32 v4, v4, v4
	v_max_f32_e32 v2, v2, v4
	s_nop 1
	v_mov_b32_e32 v160, v2
	v_mov_b32_e32 v161, v2
	s_nop 1
	v_permlane32_swap_b32_e32 v160, v161
	s_nop 1
	v_permlane32_swap_b32_e32 v161, v160
	v_mov_b32_e32 v4, v161
	s_waitcnt lgkmcnt(0)
	v_max_f32_e32 v4, v4, v4
	v_max_f32_e32 v2, v2, v4
	v_sub_f32_e32 v0, v0, v2
	v_mul_f32_e32 v0, 0x3fb8aa3b, v0
	v_exp_f32_e32 v0, v0
	s_nop 1
	v_mov_b32_dpp v160, v0 row_half_mirror row_mask:0xf bank_mask:0xf
	s_nop 1
	v_mov_b32_dpp v2, v160 quad_perm:[3,2,1,0] row_mask:0xf bank_mask:0xf
	s_waitcnt lgkmcnt(0)
	v_add_f32_e32 v2, v0, v2
	s_nop 1
	v_mov_b32_dpp v4, v2 row_ror:8 row_mask:0xf bank_mask:0xf
	s_waitcnt lgkmcnt(0)
	v_add_f32_e32 v2, v2, v4
	s_nop 1
	v_mov_b32_e32 v160, v2
	v_mov_b32_e32 v161, v2
	s_nop 1
	v_permlane16_swap_b32_e32 v160, v161
	s_nop 1
	v_permlane16_swap_b32_e32 v161, v160
	v_mov_b32_e32 v4, v161
	s_waitcnt lgkmcnt(0)
	v_add_f32_e32 v2, v2, v4
	s_nop 1
	v_mov_b32_e32 v160, v2
	v_mov_b32_e32 v161, v2
	s_nop 1
	v_permlane32_swap_b32_e32 v160, v161
	s_nop 1
	v_permlane32_swap_b32_e32 v161, v160
	v_mov_b32_e32 v4, v161
	s_and_saveexec_b64 s[14:15], s[8:9]
	s_cbranch_execz .LBB0_487
	s_waitcnt lgkmcnt(0)
	v_add_f32_e32 v2, v2, v4
	v_div_scale_f32 v4, s[40:41], v2, v2, v0
	v_rcp_f32_e32 v6, v4
	s_and_b32 s22, s26, 0xfff
	s_ashr_i32 s26, s26, 8
	s_and_b32 s26, s26, -16
	v_fma_f32 v8, -v4, v6, 1.0
	v_fmac_f32_e32 v6, v8, v6
	v_div_scale_f32 v8, vcc, v0, v2, v0
	v_mul_f32_e32 v9, v8, v6
	v_fma_f32 v10, -v4, v9, v8
	v_fmac_f32_e32 v9, v10, v6
	v_fma_f32 v4, -v4, v9, v8
	v_add_u32_e32 v8, s26, v118
	v_div_fmas_f32 v4, v4, v6, v9
	v_ashrrev_i32_e32 v9, 31, v8
	v_lshlrev_b64 v[8:9], 14, v[8:9]
	v_lshl_add_u64 v[8:9], s[18:19], 0, v[8:9]
	s_lshl_b32 s22, s22, 2
	v_div_fixup_f32 v0, v4, v2, v0
	v_lshl_add_u64 v[8:9], v[8:9], 0, s[22:23]
	global_store_dword v[8:9], v0, off

.LBB0_489:
	s_or_b64 exec, exec, s[14:15]
	v_cndmask_b32_e64 v0, v91, v1, s[0:1]
	v_cndmask_b32_e64 v1, v1, v91, s[0:1]
	s_nop 1
	v_mov_b32_e32 v160, v1
	v_mov_b32_e32 v161, v1
	s_nop 1
	v_permlane32_swap_b32_e32 v160, v161
	s_nop 1
	v_permlane32_swap_b32_e32 v161, v160
	v_mov_b32_e32 v1, v161
	v_cndmask_b32_e64 v2, v3, v93, s[0:1]
	s_nop 1
	v_mov_b32_e32 v160, v2
	v_mov_b32_e32 v161, v2
	s_nop 1
	v_permlane32_swap_b32_e32 v160, v161
	s_nop 1
	v_permlane32_swap_b32_e32 v161, v160
	v_mov_b32_e32 v2, v161
	s_waitcnt lgkmcnt(2)
	v_cndmask_b32_e64 v4, v5, v95, s[0:1]
	s_nop 1
	v_mov_b32_e32 v160, v4
	v_mov_b32_e32 v161, v4
	s_nop 1
	v_permlane32_swap_b32_e32 v160, v161
	s_nop 1
	v_permlane32_swap_b32_e32 v161, v160
	v_mov_b32_e32 v4, v161
	s_waitcnt lgkmcnt(2)
	v_add_f32_e32 v0, v0, v1
	v_cndmask_b32_e64 v1, v93, v3, s[0:1]
	s_waitcnt lgkmcnt(1)
	v_add_f32_e32 v1, v1, v2
	v_cndmask_b32_e64 v2, v95, v5, s[0:1]
	s_waitcnt lgkmcnt(0)
	v_add_f32_e32 v2, v2, v4
	v_cndmask_b32_e64 v4, v23, v97, s[0:1]
	s_nop 1
	v_mov_b32_e32 v160, v4
	v_mov_b32_e32 v161, v4
	s_nop 1
	v_permlane32_swap_b32_e32 v160, v161
	s_nop 1
	v_permlane32_swap_b32_e32 v161, v160
	v_mov_b32_e32 v4, v161
	v_cndmask_b32_e64 v5, v25, v99, s[0:1]
	s_nop 1
	v_mov_b32_e32 v160, v5
	v_mov_b32_e32 v161, v5
	s_nop 1
	v_permlane32_swap_b32_e32 v160, v161
	s_nop 1
	v_permlane32_swap_b32_e32 v161, v160
	v_mov_b32_e32 v5, v161
	v_cndmask_b32_e64 v6, v27, v101, s[0:1]
	s_nop 1
	v_mov_b32_e32 v160, v6
	v_mov_b32_e32 v161, v6
	s_nop 1
	v_permlane32_swap_b32_e32 v160, v161
	s_nop 1
	v_permlane32_swap_b32_e32 v161, v160
	v_mov_b32_e32 v6, v161
	v_cndmask_b32_e64 v8, v29, v103, s[0:1]
	v_cndmask_b32_e64 v9, v31, v7, s[0:1]
	s_nop 1
	v_mov_b32_e32 v160, v8
	v_mov_b32_e32 v161, v8
	s_nop 1
	v_permlane32_swap_b32_e32 v160, v161
	s_nop 1
	v_permlane32_swap_b32_e32 v161, v160
	v_mov_b32_e32 v8, v161
	s_nop 1
	v_mov_b32_e32 v160, v9
	v_mov_b32_e32 v161, v9
	s_nop 1
	v_permlane32_swap_b32_e32 v160, v161
	s_nop 1
	v_permlane32_swap_b32_e32 v161, v160
	v_mov_b32_e32 v9, v161
	v_cndmask_b32_e64 v3, v97, v23, s[0:1]
	s_waitcnt lgkmcnt(4)
	v_add_f32_e32 v3, v3, v4
	v_cndmask_b32_e64 v4, v99, v25, s[0:1]
	s_waitcnt lgkmcnt(3)
	v_add_f32_e32 v4, v4, v5
	v_cndmask_b32_e64 v5, v101, v27, s[0:1]
	s_waitcnt lgkmcnt(2)
	v_add_f32_e32 v5, v5, v6
	v_cndmask_b32_e64 v6, v103, v29, s[0:1]
	v_cndmask_b32_e64 v7, v7, v31, s[0:1]
	s_waitcnt lgkmcnt(1)
	v_add_f32_e32 v6, v6, v8
	s_waitcnt lgkmcnt(0)
	v_add_f32_e32 v7, v7, v9
	v_cndmask_b32_e64 v10, v0, v4, s[12:13]
	v_cndmask_b32_e64 v0, v4, v0, s[12:13]
	v_cndmask_b32_e64 v4, v5, v1, s[12:13]
	v_cndmask_b32_e64 v1, v1, v5, s[12:13]
	v_cndmask_b32_e64 v5, v2, v6, s[12:13]
	v_cndmask_b32_e64 v8, v3, v7, s[12:13]
	s_nop 1
	v_mov_b32_e32 v160, v10
	v_mov_b32_e32 v161, v10
	s_nop 1
	v_permlane16_swap_b32_e32 v160, v161
	s_nop 1
	v_permlane16_swap_b32_e32 v161, v160
	v_mov_b32_e32 v10, v161
	s_nop 1
	v_mov_b32_e32 v160, v1
	v_mov_b32_e32 v161, v1
	s_nop 1
	v_permlane16_swap_b32_e32 v160, v161
	s_nop 1
	v_permlane16_swap_b32_e32 v161, v160
	v_mov_b32_e32 v1, v161
	s_nop 1
	v_mov_b32_e32 v160, v5
	v_mov_b32_e32 v161, v5
	s_nop 1
	v_permlane16_swap_b32_e32 v160, v161
	s_nop 1
	v_permlane16_swap_b32_e32 v161, v160
	v_mov_b32_e32 v5, v161
	s_nop 1
	v_mov_b32_e32 v160, v8
	v_mov_b32_e32 v161, v8
	s_nop 1
	v_permlane16_swap_b32_e32 v160, v161
	s_nop 1
	v_permlane16_swap_b32_e32 v161, v160
	v_mov_b32_e32 v8, v161
	v_cndmask_b32_e64 v2, v6, v2, s[12:13]
	v_cndmask_b32_e64 v3, v7, v3, s[12:13]
	s_waitcnt lgkmcnt(3)
	v_add_f32_e32 v0, v0, v10
	s_waitcnt lgkmcnt(2)
	v_add_f32_e32 v1, v4, v1
	s_waitcnt lgkmcnt(1)
	v_add_f32_e32 v2, v2, v5
	s_waitcnt lgkmcnt(0)
	v_add_f32_e32 v3, v3, v8
	v_cndmask_b32_e64 v4, v0, v2, s[4:5]
	v_cndmask_b32_e64 v5, v1, v3, s[4:5]
	s_nop 1
	v_mov_b32_dpp v4, v4 row_ror:8 row_mask:0xf bank_mask:0xf
	s_nop 1
	v_mov_b32_dpp v5, v5 row_ror:8 row_mask:0xf bank_mask:0xf
	v_cndmask_b32_e64 v0, v2, v0, s[4:5]
	v_cndmask_b32_e64 v1, v3, v1, s[4:5]
	s_waitcnt lgkmcnt(1)
	v_add_f32_e32 v0, v0, v4
	s_waitcnt lgkmcnt(0)
	v_add_f32_e32 v1, v1, v5
	v_cndmask_b32_e64 v2, v0, v1, s[6:7]
	s_nop 1
	v_mov_b32_dpp v160, v2 row_half_mirror row_mask:0xf bank_mask:0xf
	s_nop 1
	v_mov_b32_dpp v2, v160 quad_perm:[3,2,1,0] row_mask:0xf bank_mask:0xf
	v_cndmask_b32_e64 v0, v1, v0, s[6:7]
	s_waitcnt lgkmcnt(0)
	v_add_f32_e32 v0, v0, v2
	s_nop 1
	v_mov_b32_dpp v1, v0 quad_perm:[2,3,0,1] row_mask:0xf bank_mask:0xf
	s_waitcnt lgkmcnt(0)
	v_add_f32_e32 v0, v0, v1
	s_nop 1
	v_mov_b32_dpp v1, v0 quad_perm:[1,0,3,2] row_mask:0xf bank_mask:0xf
	s_waitcnt lgkmcnt(0)
	v_add_f32_e32 v0, v0, v1
	s_nop 1
	v_mov_b32_dpp v160, v0 row_half_mirror row_mask:0xf bank_mask:0xf
	s_nop 1
	v_mov_b32_dpp v1, v160 quad_perm:[3,2,1,0] row_mask:0xf bank_mask:0xf
	s_waitcnt lgkmcnt(0)
	v_max_f32_e32 v1, v1, v1
	v_max_f32_e32 v1, v0, v1
	s_nop 1
	v_mov_b32_dpp v2, v1 row_ror:8 row_mask:0xf bank_mask:0xf
	s_waitcnt lgkmcnt(0)
	v_max_f32_e32 v2, v2, v2
	v_max_f32_e32 v1, v1, v2
	s_nop 1
	v_mov_b32_e32 v160, v1
	v_mov_b32_e32 v161, v1
	s_nop 1
	v_permlane16_swap_b32_e32 v160, v161
	s_nop 1
	v_permlane16_swap_b32_e32 v161, v160
	v_mov_b32_e32 v2, v161
	s_waitcnt lgkmcnt(0)
	v_max_f32_e32 v2, v2, v2
	v_max_f32_e32 v1, v1, v2
	s_nop 1
	v_mov_b32_e32 v160, v1
	v_mov_b32_e32 v161, v1
	s_nop 1
	v_permlane32_swap_b32_e32 v160, v161
	s_nop 1
	v_permlane32_swap_b32_e32 v161, v160
	v_mov_b32_e32 v2, v161
	s_waitcnt lgkmcnt(0)
	v_max_f32_e32 v2, v2, v2
	v_max_f32_e32 v1, v1, v2
	v_sub_f32_e32 v0, v0, v1
	v_mul_f32_e32 v0, 0x3fb8aa3b, v0
	v_exp_f32_e32 v0, v0
	s_nop 1
	v_mov_b32_dpp v160, v0 row_half_mirror row_mask:0xf bank_mask:0xf
	s_nop 1
	v_mov_b32_dpp v1, v160 quad_perm:[3,2,1,0] row_mask:0xf bank_mask:0xf
	s_waitcnt lgkmcnt(0)
	v_add_f32_e32 v1, v0, v1
	s_nop 1
	v_mov_b32_dpp v2, v1 row_ror:8 row_mask:0xf bank_mask:0xf
	s_waitcnt lgkmcnt(0)
	v_add_f32_e32 v1, v1, v2
	s_nop 1
	v_mov_b32_e32 v160, v1
	v_mov_b32_e32 v161, v1
	s_nop 1
	v_permlane16_swap_b32_e32 v160, v161
	s_nop 1
	v_permlane16_swap_b32_e32 v161, v160
	v_mov_b32_e32 v2, v161
	s_waitcnt lgkmcnt(0)
	v_add_f32_e32 v1, v1, v2
	s_nop 1
	v_mov_b32_e32 v160, v1
	v_mov_b32_e32 v161, v1
	s_nop 1
	v_permlane32_swap_b32_e32 v160, v161
	s_nop 1
	v_permlane32_swap_b32_e32 v161, v160
	v_mov_b32_e32 v2, v161
	s_and_saveexec_b64 s[14:15], s[8:9]
	s_cbranch_execz .LBB0_491
	s_waitcnt lgkmcnt(0)
	v_add_f32_e32 v1, v1, v2
	v_div_scale_f32 v2, s[40:41], v1, v1, v0
	v_rcp_f32_e32 v3, v2
	s_ashr_i32 s26, s30, 8
	s_and_b32 s26, s26, -16
	s_and_b32 s22, s30, 0xfff
	v_fma_f32 v4, -v2, v3, 1.0
	v_fmac_f32_e32 v3, v4, v3
	v_div_scale_f32 v4, vcc, v0, v1, v0
	v_mul_f32_e32 v5, v4, v3
	v_fma_f32 v6, -v2, v5, v4
	v_fmac_f32_e32 v5, v6, v3
	v_fma_f32 v2, -v2, v5, v4
	v_div_fmas_f32 v2, v2, v3, v5
	v_div_fixup_f32 v2, v2, v1, v0
	v_add_u32_e32 v0, s26, v118
	v_ashrrev_i32_e32 v1, 31, v0
	v_lshlrev_b64 v[0:1], 14, v[0:1]
	v_lshl_add_u64 v[0:1], s[18:19], 0, v[0:1]
	s_lshl_b32 s22, s22, 2
	v_lshl_add_u64 v[0:1], v[0:1], 0, s[22:23]
	global_store_dword v[0:1], v2, off
